# peel + nt + leading half skips the pre-barrier lgkmcnt(0) in the K-loops
# speedup vs baseline: 1.0049x; 1.0049x over previous
.LBB0_311:
	v_add_u32_e32 v100, s3, v190
	v_add_u32_e32 v156, s75, v190
	ds_read_b128 v[40:43], v100
	ds_read_b128 v[60:63], v100 offset:1024
	ds_read_b128 v[80:83], v100 offset:2048
	ds_read_b128 v[100:103], v100 offset:3072
	ds_read_b128 v[120:123], v156
	ds_read_b128 v[140:143], v156 offset:1024
	ds_read_b128 v[152:155], v156 offset:2048
	ds_read_b128 v[156:159], v156 offset:3072
	s_add_u32 s24, s0, 0xfff80080
	s_addc_u32 s25, s1, -1
	s_cmp_eq_u32 s28, 28
	s_cselect_b32 s39, s4, s25
	s_cselect_b32 s38, s5, s24
	s_cselect_b32 s25, s8, s19
	s_cselect_b32 s24, s13, s17
	v_lshl_add_u64 v[188:189], s[0:1], 0, v[168:169]
	s_add_i32 m0, s78, 0xc000
	ds_read_b128 v[172:175], v191
	ds_read_b128 v[176:179], v191 offset:1024
	ds_read_b128 v[180:183], v191 offset:2048
	ds_read_b128 v[184:187], v191 offset:3072
	ds_read_b128 v[192:195], v191 offset:4096
	ds_read_b128 v[196:199], v191 offset:5120
	ds_read_b128 v[200:203], v191 offset:6144
	ds_read_b128 v[204:207], v191 offset:7168
	global_load_lds_dwordx4 v[188:189], off
	v_lshl_add_u64 v[188:189], s[0:1], 0, v[170:171]
	s_add_i32 m0, s78, 0xe000
	s_nop 0
	global_load_lds_dwordx4 v[188:189], off
	s_waitcnt vmcnt(8)
	s_and_b64 vcc, exec, s[34:35]
	s_cbranch_vccnz .Llead_skip_0_0
	s_waitcnt lgkmcnt(0)
.Llead_skip_0_0:
	s_barrier
	s_setprio 1
	s_waitcnt lgkmcnt(0)
	v_mfma_f32_16x16x32_bf16 v[148:151], v[40:43], v[172:175], v[148:151]
	v_mfma_f32_16x16x32_bf16 v[144:147], v[80:83], v[172:175], v[144:147]
	v_mfma_f32_16x16x32_bf16 v[128:131], v[40:43], v[180:183], v[128:131]
	v_mfma_f32_16x16x32_bf16 v[124:127], v[80:83], v[180:183], v[124:127]
	v_mfma_f32_16x16x32_bf16 v[108:111], v[40:43], v[192:195], v[108:111]
	v_mfma_f32_16x16x32_bf16 v[104:107], v[80:83], v[192:195], v[104:107]
	v_mfma_f32_16x16x32_bf16 v[88:91], v[40:43], v[200:203], v[88:91]
	v_mfma_f32_16x16x32_bf16 v[84:87], v[80:83], v[200:203], v[84:87]
	v_mfma_f32_16x16x32_bf16 v[148:151], v[60:63], v[176:179], v[148:151]
	v_mfma_f32_16x16x32_bf16 v[144:147], v[100:103], v[176:179], v[144:147]
	v_mfma_f32_16x16x32_bf16 v[128:131], v[60:63], v[184:187], v[128:131]
	v_mfma_f32_16x16x32_bf16 v[124:127], v[100:103], v[184:187], v[124:127]
	v_mfma_f32_16x16x32_bf16 v[108:111], v[60:63], v[196:199], v[108:111]
	v_mfma_f32_16x16x32_bf16 v[104:107], v[100:103], v[196:199], v[104:107]
	v_mfma_f32_16x16x32_bf16 v[88:91], v[60:63], v[204:207], v[88:91]
	v_mfma_f32_16x16x32_bf16 v[84:87], v[100:103], v[204:207], v[84:87]
	s_setprio 0
	s_setprio 1
	v_mfma_f32_16x16x32_bf16 v[136:139], v[120:123], v[172:175], v[136:139]
	v_mfma_f32_16x16x32_bf16 v[132:135], v[152:155], v[172:175], v[132:135]
	v_mfma_f32_16x16x32_bf16 v[116:119], v[120:123], v[180:183], v[116:119]
	v_mfma_f32_16x16x32_bf16 v[112:115], v[152:155], v[180:183], v[112:115]
	v_mfma_f32_16x16x32_bf16 v[96:99], v[120:123], v[192:195], v[96:99]
	v_mfma_f32_16x16x32_bf16 v[92:95], v[152:155], v[192:195], v[92:95]
	v_mfma_f32_16x16x32_bf16 v[76:79], v[120:123], v[200:203], v[76:79]
	v_mfma_f32_16x16x32_bf16 v[72:75], v[152:155], v[200:203], v[72:75]
	v_mfma_f32_16x16x32_bf16 v[136:139], v[140:143], v[176:179], v[136:139]
	v_mfma_f32_16x16x32_bf16 v[132:135], v[156:159], v[176:179], v[132:135]
	v_mfma_f32_16x16x32_bf16 v[116:119], v[140:143], v[184:187], v[116:119]
	v_mfma_f32_16x16x32_bf16 v[112:115], v[156:159], v[184:187], v[112:115]
	v_mfma_f32_16x16x32_bf16 v[96:99], v[140:143], v[196:199], v[96:99]
	v_mfma_f32_16x16x32_bf16 v[92:95], v[156:159], v[196:199], v[92:95]
	v_mfma_f32_16x16x32_bf16 v[76:79], v[140:143], v[204:207], v[76:79]
	v_mfma_f32_16x16x32_bf16 v[72:75], v[156:159], v[204:207], v[72:75]
	s_setprio 0
	s_barrier
	s_mov_b32 m0, s23
	v_lshl_add_u64 v[188:189], s[24:25], 0, v[162:163]
	s_add_u32 s30, s24, 0x4000
	ds_read_b128 v[172:175], v191 offset:16384
	ds_read_b128 v[176:179], v191 offset:17408
	ds_read_b128 v[180:183], v191 offset:18432
	ds_read_b128 v[184:187], v191 offset:19456
	ds_read_b128 v[192:195], v191 offset:20480
	ds_read_b128 v[196:199], v191 offset:21504
	ds_read_b128 v[200:203], v191 offset:22528
	ds_read_b128 v[204:207], v191 offset:23552
	global_load_lds_dwordx4 v[188:189], off
	v_lshl_add_u64 v[188:189], s[24:25], 0, v[166:167]
	s_mov_b32 m0, s74
	s_addc_u32 s31, s25, 0
	global_load_lds_dwordx4 v[188:189], off
	v_lshl_add_u64 v[188:189], s[30:31], 0, v[162:163]
	s_mov_b32 m0, s76
	v_lshl_add_u64 v[208:209], s[38:39], 0, v[164:165]
	global_load_lds_dwordx4 v[188:189], off
	v_lshl_add_u64 v[188:189], s[30:31], 0, v[166:167]
	s_mov_b32 m0, s77
	s_nop 0
	global_load_lds_dwordx4 v[188:189], off
	v_lshl_add_u64 v[188:189], s[38:39], 0, v[160:161]
	s_mov_b32 m0, s78
	s_nop 0
	global_load_lds_dwordx4 v[188:189], off
	s_mov_b32 m0, s79
	s_nop 0
	global_load_lds_dwordx4 v[208:209], off
	s_waitcnt vmcnt(8)
	s_and_b64 vcc, exec, s[34:35]
	s_cbranch_vccnz .Llead_skip_0_1
	s_waitcnt lgkmcnt(0)
.Llead_skip_0_1:
	s_barrier
	s_setprio 1
	s_waitcnt lgkmcnt(0)
	v_mfma_f32_16x16x32_bf16 v[68:71], v[40:43], v[172:175], v[68:71]
	v_mfma_f32_16x16x32_bf16 v[64:67], v[80:83], v[172:175], v[64:67]
	v_mfma_f32_16x16x32_bf16 v[48:51], v[40:43], v[180:183], v[48:51]
	v_mfma_f32_16x16x32_bf16 v[44:47], v[80:83], v[180:183], v[44:47]
	v_mfma_f32_16x16x32_bf16 v[28:31], v[40:43], v[192:195], v[28:31]
	v_mfma_f32_16x16x32_bf16 v[24:27], v[80:83], v[192:195], v[24:27]
	v_mfma_f32_16x16x32_bf16 v[12:15], v[40:43], v[200:203], v[12:15]
	v_mfma_f32_16x16x32_bf16 v[8:11], v[80:83], v[200:203], v[8:11]
	v_mfma_f32_16x16x32_bf16 v[68:71], v[60:63], v[176:179], v[68:71]
	v_mfma_f32_16x16x32_bf16 v[64:67], v[100:103], v[176:179], v[64:67]
	v_mfma_f32_16x16x32_bf16 v[48:51], v[60:63], v[184:187], v[48:51]
	v_mfma_f32_16x16x32_bf16 v[44:47], v[100:103], v[184:187], v[44:47]
	v_mfma_f32_16x16x32_bf16 v[28:31], v[60:63], v[196:199], v[28:31]
	v_mfma_f32_16x16x32_bf16 v[24:27], v[100:103], v[196:199], v[24:27]
	v_mfma_f32_16x16x32_bf16 v[12:15], v[60:63], v[204:207], v[12:15]
	v_mfma_f32_16x16x32_bf16 v[8:11], v[100:103], v[204:207], v[8:11]
	s_setprio 0
	s_setprio 1
	v_mfma_f32_16x16x32_bf16 v[52:55], v[152:155], v[172:175], v[52:55]
	v_mfma_f32_16x16x32_bf16 v[36:39], v[120:123], v[180:183], v[36:39]
	v_mfma_f32_16x16x32_bf16 v[32:35], v[152:155], v[180:183], v[32:35]
	v_mfma_f32_16x16x32_bf16 v[20:23], v[120:123], v[192:195], v[20:23]
	v_mfma_f32_16x16x32_bf16 v[16:19], v[152:155], v[192:195], v[16:19]
	v_mfma_f32_16x16x32_bf16 v[4:7], v[120:123], v[200:203], v[4:7]
	v_mfma_f32_16x16x32_bf16 v[0:3], v[152:155], v[200:203], v[0:3]
	v_mfma_f32_16x16x32_bf16 v[40:43], v[120:123], v[172:175], v[56:59]
	v_mfma_f32_16x16x32_bf16 v[52:55], v[156:159], v[176:179], v[52:55]
	v_mfma_f32_16x16x32_bf16 v[36:39], v[140:143], v[184:187], v[36:39]
	v_mfma_f32_16x16x32_bf16 v[32:35], v[156:159], v[184:187], v[32:35]
	v_mfma_f32_16x16x32_bf16 v[20:23], v[140:143], v[196:199], v[20:23]
	v_mfma_f32_16x16x32_bf16 v[16:19], v[156:159], v[196:199], v[16:19]
	v_mfma_f32_16x16x32_bf16 v[4:7], v[140:143], v[204:207], v[4:7]
	v_mfma_f32_16x16x32_bf16 v[0:3], v[156:159], v[204:207], v[0:3]
	v_mfma_f32_16x16x32_bf16 v[40:43], v[140:143], v[176:179], v[40:43]
	s_setprio 0
	s_barrier
	v_add_u32_e32 v100, s86, v190
	v_add_u32_e32 v156, s95, v190
	ds_read_b128 v[56:59], v100
	ds_read_b128 v[60:63], v100 offset:1024
	ds_read_b128 v[80:83], v100 offset:2048
	ds_read_b128 v[100:103], v100 offset:3072
	ds_read_b128 v[120:123], v156
	ds_read_b128 v[140:143], v156 offset:1024
	ds_read_b128 v[152:155], v156 offset:2048
	ds_read_b128 v[156:159], v156 offset:3072
	s_add_u32 s30, s38, 0x80000
	s_addc_u32 s31, s39, 0
	s_mov_b32 m0, s82
	v_lshl_add_u64 v[210:211], s[30:31], 0, v[160:161]
	ds_read_b128 v[172:175], v191 offset:32768
	ds_read_b128 v[176:179], v191 offset:33792
	ds_read_b128 v[180:183], v191 offset:34816
	ds_read_b128 v[184:187], v191 offset:35840
	ds_read_b128 v[192:195], v191 offset:36864
	ds_read_b128 v[196:199], v191 offset:37888
	ds_read_b128 v[200:203], v191 offset:38912
	ds_read_b128 v[204:207], v191 offset:39936
	global_load_lds_dwordx4 v[210:211], off
	v_lshl_add_u64 v[210:211], s[30:31], 0, v[164:165]
	s_mov_b32 m0, s83
	s_nop 0
	global_load_lds_dwordx4 v[210:211], off
	s_waitcnt vmcnt(8)
	s_and_b64 vcc, exec, s[34:35]
	s_cbranch_vccnz .Llead_skip_0_2
	s_waitcnt lgkmcnt(0)
.Llead_skip_0_2:
	s_barrier
	s_setprio 1
	s_waitcnt lgkmcnt(0)
	v_mfma_f32_16x16x32_bf16 v[148:151], v[56:59], v[172:175], v[148:151]
	v_mfma_f32_16x16x32_bf16 v[144:147], v[80:83], v[172:175], v[144:147]
	v_mfma_f32_16x16x32_bf16 v[128:131], v[56:59], v[180:183], v[128:131]
	v_mfma_f32_16x16x32_bf16 v[124:127], v[80:83], v[180:183], v[124:127]
	v_mfma_f32_16x16x32_bf16 v[108:111], v[56:59], v[192:195], v[108:111]
	v_mfma_f32_16x16x32_bf16 v[104:107], v[80:83], v[192:195], v[104:107]
	v_mfma_f32_16x16x32_bf16 v[88:91], v[56:59], v[200:203], v[88:91]
	v_mfma_f32_16x16x32_bf16 v[84:87], v[80:83], v[200:203], v[84:87]
	v_mfma_f32_16x16x32_bf16 v[148:151], v[60:63], v[176:179], v[148:151]
	v_mfma_f32_16x16x32_bf16 v[144:147], v[100:103], v[176:179], v[144:147]
	v_mfma_f32_16x16x32_bf16 v[128:131], v[60:63], v[184:187], v[128:131]
	v_mfma_f32_16x16x32_bf16 v[124:127], v[100:103], v[184:187], v[124:127]
	v_mfma_f32_16x16x32_bf16 v[108:111], v[60:63], v[196:199], v[108:111]
	v_mfma_f32_16x16x32_bf16 v[104:107], v[100:103], v[196:199], v[104:107]
	v_mfma_f32_16x16x32_bf16 v[88:91], v[60:63], v[204:207], v[88:91]
	v_mfma_f32_16x16x32_bf16 v[84:87], v[100:103], v[204:207], v[84:87]
	s_setprio 0
	s_setprio 1
	v_mfma_f32_16x16x32_bf16 v[136:139], v[120:123], v[172:175], v[136:139]
	v_mfma_f32_16x16x32_bf16 v[132:135], v[152:155], v[172:175], v[132:135]
	v_mfma_f32_16x16x32_bf16 v[116:119], v[120:123], v[180:183], v[116:119]
	v_mfma_f32_16x16x32_bf16 v[112:115], v[152:155], v[180:183], v[112:115]
	v_mfma_f32_16x16x32_bf16 v[96:99], v[120:123], v[192:195], v[96:99]
	v_mfma_f32_16x16x32_bf16 v[92:95], v[152:155], v[192:195], v[92:95]
	v_mfma_f32_16x16x32_bf16 v[76:79], v[120:123], v[200:203], v[76:79]
	v_mfma_f32_16x16x32_bf16 v[72:75], v[152:155], v[200:203], v[72:75]
	v_mfma_f32_16x16x32_bf16 v[136:139], v[140:143], v[176:179], v[136:139]
	v_mfma_f32_16x16x32_bf16 v[132:135], v[156:159], v[176:179], v[132:135]
	v_mfma_f32_16x16x32_bf16 v[116:119], v[140:143], v[184:187], v[116:119]
	v_mfma_f32_16x16x32_bf16 v[112:115], v[156:159], v[184:187], v[112:115]
	v_mfma_f32_16x16x32_bf16 v[96:99], v[140:143], v[196:199], v[96:99]
	v_mfma_f32_16x16x32_bf16 v[92:95], v[156:159], v[196:199], v[92:95]
	v_mfma_f32_16x16x32_bf16 v[76:79], v[140:143], v[204:207], v[76:79]
	v_mfma_f32_16x16x32_bf16 v[72:75], v[156:159], v[204:207], v[72:75]
	s_setprio 0
	s_barrier
	s_add_u32 s30, s24, 0x8000
	s_addc_u32 s31, s25, 0
	s_mov_b32 m0, s87
	v_lshl_add_u64 v[210:211], s[30:31], 0, v[162:163]
	s_add_u32 s24, s24, 0xc000
	ds_read_b128 v[172:175], v191 offset:49152
	ds_read_b128 v[176:179], v191 offset:50176
	ds_read_b128 v[180:183], v191 offset:51200
	ds_read_b128 v[184:187], v191 offset:52224
	ds_read_b128 v[192:195], v191 offset:53248
	ds_read_b128 v[196:199], v191 offset:54272
	ds_read_b128 v[200:203], v191 offset:55296
	ds_read_b128 v[204:207], v191 offset:56320
	global_load_lds_dwordx4 v[210:211], off
	v_lshl_add_u64 v[210:211], s[30:31], 0, v[166:167]
	s_mov_b32 m0, s92
	s_addc_u32 s25, s25, 0
	global_load_lds_dwordx4 v[210:211], off
	v_lshl_add_u64 v[210:211], s[24:25], 0, v[162:163]
	s_mov_b32 m0, s96
	v_lshl_add_u64 v[188:189], v[188:189], 0, s[26:27]
	global_load_lds_dwordx4 v[210:211], off
	v_lshl_add_u64 v[210:211], s[24:25], 0, v[166:167]
	s_mov_b32 m0, s97
	s_nop 0
	global_load_lds_dwordx4 v[210:211], off
	s_mov_b32 m0, s93
	s_nop 0
	global_load_lds_dwordx4 v[188:189], off
	v_lshl_add_u64 v[188:189], v[208:209], 0, s[26:27]
	s_mov_b32 m0, s94
	s_nop 0
	global_load_lds_dwordx4 v[188:189], off
	s_waitcnt vmcnt(8)
	s_and_b64 vcc, exec, s[34:35]
	s_cbranch_vccnz .Llead_skip_0_3
	s_waitcnt lgkmcnt(0)
.Llead_skip_0_3:
	s_barrier
	s_setprio 1
	s_waitcnt lgkmcnt(0)
	v_mfma_f32_16x16x32_bf16 v[68:71], v[56:59], v[172:175], v[68:71]
	v_mfma_f32_16x16x32_bf16 v[64:67], v[80:83], v[172:175], v[64:67]
	v_mfma_f32_16x16x32_bf16 v[48:51], v[56:59], v[180:183], v[48:51]
	v_mfma_f32_16x16x32_bf16 v[44:47], v[80:83], v[180:183], v[44:47]
	v_mfma_f32_16x16x32_bf16 v[28:31], v[56:59], v[192:195], v[28:31]
	v_mfma_f32_16x16x32_bf16 v[24:27], v[80:83], v[192:195], v[24:27]
	v_mfma_f32_16x16x32_bf16 v[12:15], v[56:59], v[200:203], v[12:15]
	v_mfma_f32_16x16x32_bf16 v[8:11], v[80:83], v[200:203], v[8:11]
	v_mfma_f32_16x16x32_bf16 v[68:71], v[60:63], v[176:179], v[68:71]
	v_mfma_f32_16x16x32_bf16 v[64:67], v[100:103], v[176:179], v[64:67]
	v_mfma_f32_16x16x32_bf16 v[48:51], v[60:63], v[184:187], v[48:51]
	v_mfma_f32_16x16x32_bf16 v[44:47], v[100:103], v[184:187], v[44:47]
	v_mfma_f32_16x16x32_bf16 v[28:31], v[60:63], v[196:199], v[28:31]
	v_mfma_f32_16x16x32_bf16 v[24:27], v[100:103], v[196:199], v[24:27]
	v_mfma_f32_16x16x32_bf16 v[12:15], v[60:63], v[204:207], v[12:15]
	v_mfma_f32_16x16x32_bf16 v[8:11], v[100:103], v[204:207], v[8:11]
	s_setprio 0
	s_setprio 1
	v_mfma_f32_16x16x32_bf16 v[40:43], v[120:123], v[172:175], v[40:43]
	v_mfma_f32_16x16x32_bf16 v[56:59], v[140:143], v[176:179], v[40:43]
	v_mfma_f32_16x16x32_bf16 v[40:43], v[152:155], v[172:175], v[52:55]
	v_mfma_f32_16x16x32_bf16 v[36:39], v[120:123], v[180:183], v[36:39]
	v_mfma_f32_16x16x32_bf16 v[32:35], v[152:155], v[180:183], v[32:35]
	v_mfma_f32_16x16x32_bf16 v[20:23], v[120:123], v[192:195], v[20:23]
	v_mfma_f32_16x16x32_bf16 v[16:19], v[152:155], v[192:195], v[16:19]
	v_mfma_f32_16x16x32_bf16 v[4:7], v[120:123], v[200:203], v[4:7]
	v_mfma_f32_16x16x32_bf16 v[0:3], v[152:155], v[200:203], v[0:3]
	v_mfma_f32_16x16x32_bf16 v[52:55], v[156:159], v[176:179], v[40:43]
	v_mfma_f32_16x16x32_bf16 v[36:39], v[140:143], v[184:187], v[36:39]
	v_mfma_f32_16x16x32_bf16 v[32:35], v[156:159], v[184:187], v[32:35]
	v_mfma_f32_16x16x32_bf16 v[20:23], v[140:143], v[196:199], v[20:23]
	v_mfma_f32_16x16x32_bf16 v[16:19], v[156:159], v[196:199], v[16:19]
	v_mfma_f32_16x16x32_bf16 v[4:7], v[140:143], v[204:207], v[4:7]
	v_mfma_f32_16x16x32_bf16 v[0:3], v[156:159], v[204:207], v[0:3]
	s_setprio 0
	s_barrier
	s_add_i32 s28, s28, 2
	s_add_u32 s17, s17, 0x10000
	s_addc_u32 s19, s19, 0
	s_add_u32 s0, s0, 0x100
	s_addc_u32 s1, s1, 0
	s_cmp_gt_u32 s28, 29
	s_cbranch_scc0 .LBB0_311
	s_and_b64 vcc, exec, s[34:35]
	s_cbranch_vccz .LBB0_314
	s_barrier

.LBB0_1055:
	v_add_u32_e32 v140, s28, v215
	v_add_u32_e32 v156, s54, v215
	ds_read_b128 v[128:131], v140
	ds_read_b128 v[132:135], v140 offset:1024
	ds_read_b128 v[136:139], v140 offset:2048
	ds_read_b128 v[140:143], v140 offset:3072
	ds_read_b128 v[144:147], v156
	ds_read_b128 v[148:151], v156 offset:1024
	ds_read_b128 v[152:155], v156 offset:2048
	ds_read_b128 v[156:159], v156 offset:3072
	s_add_u32 s50, s0, 0xfff80080
	s_addc_u32 s51, s1, -1
	s_cmp_eq_u32 s80, 28
	s_cselect_b32 s53, s4, s51
	s_cselect_b32 s52, s5, s50
	s_cselect_b32 s51, s39, s55
	s_cselect_b32 s50, s41, s49
	v_lshl_add_u64 v[204:205], s[0:1], 0, v[180:181]
	s_add_i32 m0, s58, 0xc000
	ds_read_b128 v[160:163], v251
	ds_read_b128 v[164:167], v251 offset:1024
	ds_read_b128 v[168:171], v251 offset:2048
	ds_read_b128 v[184:187], v251 offset:3072
	ds_read_b128 v[188:191], v251 offset:4096
	ds_read_b128 v[192:195], v251 offset:5120
	ds_read_b128 v[196:199], v251 offset:6144
	ds_read_b128 v[200:203], v251 offset:7168
	global_load_lds_dwordx4 v[204:205], off
	v_lshl_add_u64 v[204:205], s[0:1], 0, v[182:183]
	s_add_i32 m0, s58, 0xe000
	s_nop 0
	global_load_lds_dwordx4 v[204:205], off
	s_waitcnt vmcnt(8)
	s_and_b64 vcc, exec, s[34:35]
	s_cbranch_vccnz .Llead_skip_1_0
	s_waitcnt lgkmcnt(0)
.Llead_skip_1_0:
	s_barrier
	s_setprio 1
	s_waitcnt lgkmcnt(0)
	v_mfma_f32_16x16x32_bf16 v[124:127], v[128:131], v[160:163], v[124:127]
	v_mfma_f32_16x16x32_bf16 v[120:123], v[136:139], v[160:163], v[120:123]
	v_mfma_f32_16x16x32_bf16 v[116:119], v[128:131], v[168:171], v[116:119]
	v_mfma_f32_16x16x32_bf16 v[112:115], v[136:139], v[168:171], v[112:115]
	v_mfma_f32_16x16x32_bf16 v[108:111], v[128:131], v[188:191], v[108:111]
	v_mfma_f32_16x16x32_bf16 v[104:107], v[136:139], v[188:191], v[104:107]
	v_mfma_f32_16x16x32_bf16 v[100:103], v[128:131], v[196:199], v[100:103]
	v_mfma_f32_16x16x32_bf16 v[96:99], v[136:139], v[196:199], v[96:99]
	v_mfma_f32_16x16x32_bf16 v[124:127], v[132:135], v[164:167], v[124:127]
	v_mfma_f32_16x16x32_bf16 v[120:123], v[140:143], v[164:167], v[120:123]
	v_mfma_f32_16x16x32_bf16 v[116:119], v[132:135], v[184:187], v[116:119]
	v_mfma_f32_16x16x32_bf16 v[112:115], v[140:143], v[184:187], v[112:115]
	v_mfma_f32_16x16x32_bf16 v[108:111], v[132:135], v[192:195], v[108:111]
	v_mfma_f32_16x16x32_bf16 v[104:107], v[140:143], v[192:195], v[104:107]
	v_mfma_f32_16x16x32_bf16 v[100:103], v[132:135], v[200:203], v[100:103]
	v_mfma_f32_16x16x32_bf16 v[96:99], v[140:143], v[200:203], v[96:99]
	s_setprio 0
	s_setprio 1
	v_mfma_f32_16x16x32_bf16 v[60:63], v[144:147], v[160:163], v[60:63]
	v_mfma_f32_16x16x32_bf16 v[56:59], v[152:155], v[160:163], v[56:59]
	v_mfma_f32_16x16x32_bf16 v[52:55], v[144:147], v[168:171], v[52:55]
	v_mfma_f32_16x16x32_bf16 v[48:51], v[152:155], v[168:171], v[48:51]
	v_mfma_f32_16x16x32_bf16 v[44:47], v[144:147], v[188:191], v[44:47]
	v_mfma_f32_16x16x32_bf16 v[40:43], v[152:155], v[188:191], v[40:43]
	v_mfma_f32_16x16x32_bf16 v[36:39], v[144:147], v[196:199], v[36:39]
	v_mfma_f32_16x16x32_bf16 v[32:35], v[152:155], v[196:199], v[32:35]
	v_mfma_f32_16x16x32_bf16 v[60:63], v[148:151], v[164:167], v[60:63]
	v_mfma_f32_16x16x32_bf16 v[56:59], v[156:159], v[164:167], v[56:59]
	v_mfma_f32_16x16x32_bf16 v[52:55], v[148:151], v[184:187], v[52:55]
	v_mfma_f32_16x16x32_bf16 v[48:51], v[156:159], v[184:187], v[48:51]
	v_mfma_f32_16x16x32_bf16 v[44:47], v[148:151], v[192:195], v[44:47]
	v_mfma_f32_16x16x32_bf16 v[40:43], v[156:159], v[192:195], v[40:43]
	v_mfma_f32_16x16x32_bf16 v[36:39], v[148:151], v[200:203], v[36:39]
	v_mfma_f32_16x16x32_bf16 v[32:35], v[156:159], v[200:203], v[32:35]
	s_setprio 0
	s_barrier
	s_mov_b32 m0, s30
	v_lshl_add_u64 v[204:205], s[50:51], 0, v[174:175]
	s_add_u32 s82, s50, 0x4000
	ds_read_b128 v[160:163], v251 offset:16384
	ds_read_b128 v[164:167], v251 offset:17408
	ds_read_b128 v[168:171], v251 offset:18432
	ds_read_b128 v[184:187], v251 offset:19456
	ds_read_b128 v[188:191], v251 offset:20480
	ds_read_b128 v[192:195], v251 offset:21504
	ds_read_b128 v[196:199], v251 offset:22528
	ds_read_b128 v[200:203], v251 offset:23552
	global_load_lds_dwordx4 v[204:205], off
	v_lshl_add_u64 v[204:205], s[50:51], 0, v[178:179]
	s_mov_b32 m0, s43
	s_addc_u32 s83, s51, 0
	global_load_lds_dwordx4 v[204:205], off
	v_lshl_add_u64 v[204:205], s[82:83], 0, v[174:175]
	s_mov_b32 m0, s56
	v_lshl_add_u64 v[206:207], s[52:53], 0, v[176:177]
	global_load_lds_dwordx4 v[204:205], off
	v_lshl_add_u64 v[204:205], s[82:83], 0, v[178:179]
	s_mov_b32 m0, s57
	s_nop 0
	global_load_lds_dwordx4 v[204:205], off
	v_lshl_add_u64 v[204:205], s[52:53], 0, v[172:173]
	s_mov_b32 m0, s58
	s_nop 0
	global_load_lds_dwordx4 v[204:205], off
	s_mov_b32 m0, s59
	s_nop 0
	global_load_lds_dwordx4 v[206:207], off
	s_waitcnt vmcnt(8)
	s_and_b64 vcc, exec, s[34:35]
	s_cbranch_vccnz .Llead_skip_1_1
	s_waitcnt lgkmcnt(0)
.Llead_skip_1_1:
	s_barrier
	s_setprio 1
	s_waitcnt lgkmcnt(0)
	v_mfma_f32_16x16x32_bf16 v[92:95], v[128:131], v[160:163], v[92:95]
	v_mfma_f32_16x16x32_bf16 v[88:91], v[136:139], v[160:163], v[88:91]
	v_mfma_f32_16x16x32_bf16 v[84:87], v[128:131], v[168:171], v[84:87]
	v_mfma_f32_16x16x32_bf16 v[80:83], v[136:139], v[168:171], v[80:83]
	v_mfma_f32_16x16x32_bf16 v[76:79], v[128:131], v[188:191], v[76:79]
	v_mfma_f32_16x16x32_bf16 v[72:75], v[136:139], v[188:191], v[72:75]
	v_mfma_f32_16x16x32_bf16 v[68:71], v[128:131], v[196:199], v[68:71]
	v_mfma_f32_16x16x32_bf16 v[64:67], v[136:139], v[196:199], v[64:67]
	v_mfma_f32_16x16x32_bf16 v[92:95], v[132:135], v[164:167], v[92:95]
	v_mfma_f32_16x16x32_bf16 v[88:91], v[140:143], v[164:167], v[88:91]
	v_mfma_f32_16x16x32_bf16 v[84:87], v[132:135], v[184:187], v[84:87]
	v_mfma_f32_16x16x32_bf16 v[80:83], v[140:143], v[184:187], v[80:83]
	v_mfma_f32_16x16x32_bf16 v[76:79], v[132:135], v[192:195], v[76:79]
	v_mfma_f32_16x16x32_bf16 v[72:75], v[140:143], v[192:195], v[72:75]
	v_mfma_f32_16x16x32_bf16 v[68:71], v[132:135], v[200:203], v[68:71]
	v_mfma_f32_16x16x32_bf16 v[64:67], v[140:143], v[200:203], v[64:67]
	s_setprio 0
	s_setprio 1
	v_mfma_f32_16x16x32_bf16 v[28:31], v[144:147], v[160:163], v[28:31]
	v_mfma_f32_16x16x32_bf16 v[24:27], v[152:155], v[160:163], v[24:27]
	v_mfma_f32_16x16x32_bf16 v[20:23], v[144:147], v[168:171], v[20:23]
	v_mfma_f32_16x16x32_bf16 v[16:19], v[152:155], v[168:171], v[16:19]
	v_mfma_f32_16x16x32_bf16 v[12:15], v[144:147], v[188:191], v[12:15]
	v_mfma_f32_16x16x32_bf16 v[8:11], v[152:155], v[188:191], v[8:11]
	v_mfma_f32_16x16x32_bf16 v[4:7], v[144:147], v[196:199], v[4:7]
	v_mfma_f32_16x16x32_bf16 v[0:3], v[152:155], v[196:199], v[0:3]
	v_mfma_f32_16x16x32_bf16 v[28:31], v[148:151], v[164:167], v[28:31]
	v_mfma_f32_16x16x32_bf16 v[24:27], v[156:159], v[164:167], v[24:27]
	v_mfma_f32_16x16x32_bf16 v[20:23], v[148:151], v[184:187], v[20:23]
	v_mfma_f32_16x16x32_bf16 v[16:19], v[156:159], v[184:187], v[16:19]
	v_mfma_f32_16x16x32_bf16 v[12:15], v[148:151], v[192:195], v[12:15]
	v_mfma_f32_16x16x32_bf16 v[8:11], v[156:159], v[192:195], v[8:11]
	v_mfma_f32_16x16x32_bf16 v[4:7], v[148:151], v[200:203], v[4:7]
	v_mfma_f32_16x16x32_bf16 v[0:3], v[156:159], v[200:203], v[0:3]
	s_setprio 0
	s_barrier
	v_add_u32_e32 v140, s68, v215
	v_add_u32_e32 v156, s73, v215
	ds_read_b128 v[128:131], v140
	ds_read_b128 v[132:135], v140 offset:1024
	ds_read_b128 v[136:139], v140 offset:2048
	ds_read_b128 v[140:143], v140 offset:3072
	ds_read_b128 v[144:147], v156
	ds_read_b128 v[148:151], v156 offset:1024
	ds_read_b128 v[152:155], v156 offset:2048
	ds_read_b128 v[156:159], v156 offset:3072
	s_add_u32 s52, s52, 0x80000
	s_addc_u32 s53, s53, 0
	s_mov_b32 m0, s60
	v_lshl_add_u64 v[208:209], s[52:53], 0, v[172:173]
	ds_read_b128 v[160:163], v251 offset:32768
	ds_read_b128 v[164:167], v251 offset:33792
	ds_read_b128 v[168:171], v251 offset:34816
	ds_read_b128 v[184:187], v251 offset:35840
	ds_read_b128 v[188:191], v251 offset:36864
	ds_read_b128 v[192:195], v251 offset:37888
	ds_read_b128 v[196:199], v251 offset:38912
	ds_read_b128 v[200:203], v251 offset:39936
	global_load_lds_dwordx4 v[208:209], off
	v_lshl_add_u64 v[208:209], s[52:53], 0, v[176:177]
	s_mov_b32 m0, s61
	s_nop 0
	global_load_lds_dwordx4 v[208:209], off
	s_waitcnt vmcnt(8)
	s_and_b64 vcc, exec, s[34:35]
	s_cbranch_vccnz .Llead_skip_1_2
	s_waitcnt lgkmcnt(0)
.Llead_skip_1_2:
	s_barrier
	s_setprio 1
	s_waitcnt lgkmcnt(0)
	v_mfma_f32_16x16x32_bf16 v[124:127], v[128:131], v[160:163], v[124:127]
	v_mfma_f32_16x16x32_bf16 v[120:123], v[136:139], v[160:163], v[120:123]
	v_mfma_f32_16x16x32_bf16 v[116:119], v[128:131], v[168:171], v[116:119]
	v_mfma_f32_16x16x32_bf16 v[112:115], v[136:139], v[168:171], v[112:115]
	v_mfma_f32_16x16x32_bf16 v[108:111], v[128:131], v[188:191], v[108:111]
	v_mfma_f32_16x16x32_bf16 v[104:107], v[136:139], v[188:191], v[104:107]
	v_mfma_f32_16x16x32_bf16 v[100:103], v[128:131], v[196:199], v[100:103]
	v_mfma_f32_16x16x32_bf16 v[96:99], v[136:139], v[196:199], v[96:99]
	v_mfma_f32_16x16x32_bf16 v[124:127], v[132:135], v[164:167], v[124:127]
	v_mfma_f32_16x16x32_bf16 v[120:123], v[140:143], v[164:167], v[120:123]
	v_mfma_f32_16x16x32_bf16 v[116:119], v[132:135], v[184:187], v[116:119]
	v_mfma_f32_16x16x32_bf16 v[112:115], v[140:143], v[184:187], v[112:115]
	v_mfma_f32_16x16x32_bf16 v[108:111], v[132:135], v[192:195], v[108:111]
	v_mfma_f32_16x16x32_bf16 v[104:107], v[140:143], v[192:195], v[104:107]
	v_mfma_f32_16x16x32_bf16 v[100:103], v[132:135], v[200:203], v[100:103]
	v_mfma_f32_16x16x32_bf16 v[96:99], v[140:143], v[200:203], v[96:99]
	s_setprio 0
	s_setprio 1
	v_mfma_f32_16x16x32_bf16 v[60:63], v[144:147], v[160:163], v[60:63]
	v_mfma_f32_16x16x32_bf16 v[56:59], v[152:155], v[160:163], v[56:59]
	v_mfma_f32_16x16x32_bf16 v[52:55], v[144:147], v[168:171], v[52:55]
	v_mfma_f32_16x16x32_bf16 v[48:51], v[152:155], v[168:171], v[48:51]
	v_mfma_f32_16x16x32_bf16 v[44:47], v[144:147], v[188:191], v[44:47]
	v_mfma_f32_16x16x32_bf16 v[40:43], v[152:155], v[188:191], v[40:43]
	v_mfma_f32_16x16x32_bf16 v[36:39], v[144:147], v[196:199], v[36:39]
	v_mfma_f32_16x16x32_bf16 v[32:35], v[152:155], v[196:199], v[32:35]
	v_mfma_f32_16x16x32_bf16 v[60:63], v[148:151], v[164:167], v[60:63]
	v_mfma_f32_16x16x32_bf16 v[56:59], v[156:159], v[164:167], v[56:59]
	v_mfma_f32_16x16x32_bf16 v[52:55], v[148:151], v[184:187], v[52:55]
	v_mfma_f32_16x16x32_bf16 v[48:51], v[156:159], v[184:187], v[48:51]
	v_mfma_f32_16x16x32_bf16 v[44:47], v[148:151], v[192:195], v[44:47]
	v_mfma_f32_16x16x32_bf16 v[40:43], v[156:159], v[192:195], v[40:43]
	v_mfma_f32_16x16x32_bf16 v[36:39], v[148:151], v[200:203], v[36:39]
	v_mfma_f32_16x16x32_bf16 v[32:35], v[156:159], v[200:203], v[32:35]
	s_setprio 0
	s_barrier
	s_add_u32 s52, s50, 0x8000
	s_addc_u32 s53, s51, 0
	s_mov_b32 m0, s69
	v_lshl_add_u64 v[208:209], s[52:53], 0, v[174:175]
	s_add_u32 s50, s50, 0xc000
	ds_read_b128 v[160:163], v251 offset:49152
	ds_read_b128 v[164:167], v251 offset:50176
	ds_read_b128 v[168:171], v251 offset:51200
	ds_read_b128 v[184:187], v251 offset:52224
	ds_read_b128 v[188:191], v251 offset:53248
	ds_read_b128 v[192:195], v251 offset:54272
	ds_read_b128 v[196:199], v251 offset:55296
	ds_read_b128 v[200:203], v251 offset:56320
	global_load_lds_dwordx4 v[208:209], off
	v_lshl_add_u64 v[208:209], s[52:53], 0, v[178:179]
	s_mov_b32 m0, s70
	s_addc_u32 s51, s51, 0
	global_load_lds_dwordx4 v[208:209], off
	v_lshl_add_u64 v[208:209], s[50:51], 0, v[174:175]
	s_mov_b32 m0, s74
	v_lshl_add_u64 v[204:205], v[204:205], 0, s[26:27]
	global_load_lds_dwordx4 v[208:209], off
	v_lshl_add_u64 v[208:209], s[50:51], 0, v[178:179]
	s_mov_b32 m0, s75
	s_nop 0
	global_load_lds_dwordx4 v[208:209], off
	s_mov_b32 m0, s71
	s_nop 0
	global_load_lds_dwordx4 v[204:205], off
	v_lshl_add_u64 v[204:205], v[206:207], 0, s[26:27]
	s_mov_b32 m0, s72
	s_nop 0
	global_load_lds_dwordx4 v[204:205], off
	s_waitcnt vmcnt(8)
	s_and_b64 vcc, exec, s[34:35]
	s_cbranch_vccnz .Llead_skip_1_3
	s_waitcnt lgkmcnt(0)
.Llead_skip_1_3:
	s_barrier
	s_setprio 1
	s_waitcnt lgkmcnt(0)
	v_mfma_f32_16x16x32_bf16 v[92:95], v[128:131], v[160:163], v[92:95]
	v_mfma_f32_16x16x32_bf16 v[88:91], v[136:139], v[160:163], v[88:91]
	v_mfma_f32_16x16x32_bf16 v[84:87], v[128:131], v[168:171], v[84:87]
	v_mfma_f32_16x16x32_bf16 v[80:83], v[136:139], v[168:171], v[80:83]
	v_mfma_f32_16x16x32_bf16 v[76:79], v[128:131], v[188:191], v[76:79]
	v_mfma_f32_16x16x32_bf16 v[72:75], v[136:139], v[188:191], v[72:75]
	v_mfma_f32_16x16x32_bf16 v[68:71], v[128:131], v[196:199], v[68:71]
	v_mfma_f32_16x16x32_bf16 v[64:67], v[136:139], v[196:199], v[64:67]
	v_mfma_f32_16x16x32_bf16 v[92:95], v[132:135], v[164:167], v[92:95]
	v_mfma_f32_16x16x32_bf16 v[88:91], v[140:143], v[164:167], v[88:91]
	v_mfma_f32_16x16x32_bf16 v[84:87], v[132:135], v[184:187], v[84:87]
	v_mfma_f32_16x16x32_bf16 v[80:83], v[140:143], v[184:187], v[80:83]
	v_mfma_f32_16x16x32_bf16 v[76:79], v[132:135], v[192:195], v[76:79]
	v_mfma_f32_16x16x32_bf16 v[72:75], v[140:143], v[192:195], v[72:75]
	v_mfma_f32_16x16x32_bf16 v[68:71], v[132:135], v[200:203], v[68:71]
	v_mfma_f32_16x16x32_bf16 v[64:67], v[140:143], v[200:203], v[64:67]
	s_setprio 0
	s_setprio 1
	v_mfma_f32_16x16x32_bf16 v[28:31], v[144:147], v[160:163], v[28:31]
	v_mfma_f32_16x16x32_bf16 v[24:27], v[152:155], v[160:163], v[24:27]
	v_mfma_f32_16x16x32_bf16 v[20:23], v[144:147], v[168:171], v[20:23]
	v_mfma_f32_16x16x32_bf16 v[16:19], v[152:155], v[168:171], v[16:19]
	v_mfma_f32_16x16x32_bf16 v[12:15], v[144:147], v[188:191], v[12:15]
	v_mfma_f32_16x16x32_bf16 v[8:11], v[152:155], v[188:191], v[8:11]
	v_mfma_f32_16x16x32_bf16 v[4:7], v[144:147], v[196:199], v[4:7]
	v_mfma_f32_16x16x32_bf16 v[0:3], v[152:155], v[196:199], v[0:3]
	v_mfma_f32_16x16x32_bf16 v[28:31], v[148:151], v[164:167], v[28:31]
	v_mfma_f32_16x16x32_bf16 v[24:27], v[156:159], v[164:167], v[24:27]
	v_mfma_f32_16x16x32_bf16 v[20:23], v[148:151], v[184:187], v[20:23]
	v_mfma_f32_16x16x32_bf16 v[16:19], v[156:159], v[184:187], v[16:19]
	v_mfma_f32_16x16x32_bf16 v[12:15], v[148:151], v[192:195], v[12:15]
	v_mfma_f32_16x16x32_bf16 v[8:11], v[156:159], v[192:195], v[8:11]
	v_mfma_f32_16x16x32_bf16 v[4:7], v[148:151], v[200:203], v[4:7]
	v_mfma_f32_16x16x32_bf16 v[0:3], v[156:159], v[200:203], v[0:3]
	s_setprio 0
	s_barrier
	s_add_i32 s80, s80, 2
	s_add_u32 s49, s49, 0x10000
	s_addc_u32 s55, s55, 0
	s_add_u32 s0, s0, 0x100
	s_addc_u32 s1, s1, 0
	s_cmp_gt_u32 s80, 29
	s_cbranch_scc0 .LBB0_1055
	v_mov_b64_e32 v[220:221], 0x1ff
	v_mov_b64_e32 v[218:219], 0x200
	s_and_b64 vcc, exec, s[34:35]
	s_cbranch_vccz .LBB0_1058
	s_barrier

.LBB0_1173:
	v_add_u32_e32 v124, s28, v156
	v_add_u32_e32 v170, s45, v156
	ds_read_b128 v[108:111], v124
	ds_read_b128 v[112:115], v124 offset:1024
	ds_read_b128 v[120:123], v124 offset:2048
	ds_read_b128 v[124:127], v124 offset:3072
	ds_read_b128 v[158:161], v170
	ds_read_b128 v[162:165], v170 offset:1024
	ds_read_b128 v[166:169], v170 offset:2048
	ds_read_b128 v[170:173], v170 offset:3072
	s_add_u32 s46, s0, 0x10000
	s_addc_u32 s47, s1, 0
	s_cmp_eq_u32 s78, 28
	s_cselect_b32 s52, s5, s46
	s_cselect_b32 s53, s4, s47
	s_cselect_b32 s50, s39, s76
	s_cselect_b32 s51, s35, s77
	s_add_u32 s48, s52, 0x8000
	s_addc_u32 s49, s53, 0
	v_lshl_add_u64 v[206:207], s[0:1], 0, v[152:153]
	s_add_i32 m0, s56, 0xc000
	ds_read_b128 v[174:177], v157
	ds_read_b128 v[178:181], v157 offset:1024
	ds_read_b128 v[182:185], v157 offset:2048
	ds_read_b128 v[186:189], v157 offset:3072
	ds_read_b128 v[190:193], v157 offset:4096
	ds_read_b128 v[194:197], v157 offset:5120
	ds_read_b128 v[198:201], v157 offset:6144
	ds_read_b128 v[202:205], v157 offset:7168
	global_load_lds_dwordx4 v[206:207], off
	v_lshl_add_u64 v[206:207], s[0:1], 0, v[154:155]
	s_add_i32 m0, s56, 0xe000
	s_nop 0
	global_load_lds_dwordx4 v[206:207], off
	s_waitcnt vmcnt(8)
	s_and_b64 vcc, exec, s[24:25]
	s_cbranch_vccnz .Llead_skip_2_0
	s_waitcnt lgkmcnt(0)
.Llead_skip_2_0:
	s_barrier
	s_setprio 1
	s_waitcnt lgkmcnt(0)
	v_mfma_f32_16x16x32_bf16 v[140:143], v[108:111], v[174:177], v[140:143]
	v_mfma_f32_16x16x32_bf16 v[136:139], v[120:123], v[174:177], v[136:139]
	v_mfma_f32_16x16x32_bf16 v[116:119], v[108:111], v[182:185], v[116:119]
	v_mfma_f32_16x16x32_bf16 v[104:107], v[120:123], v[182:185], v[104:107]
	v_mfma_f32_16x16x32_bf16 v[92:95], v[108:111], v[190:193], v[92:95]
	v_mfma_f32_16x16x32_bf16 v[88:91], v[120:123], v[190:193], v[88:91]
	v_mfma_f32_16x16x32_bf16 v[76:79], v[108:111], v[198:201], v[76:79]
	v_mfma_f32_16x16x32_bf16 v[72:75], v[120:123], v[198:201], v[72:75]
	v_mfma_f32_16x16x32_bf16 v[140:143], v[112:115], v[178:181], v[140:143]
	v_mfma_f32_16x16x32_bf16 v[136:139], v[124:127], v[178:181], v[136:139]
	v_mfma_f32_16x16x32_bf16 v[116:119], v[112:115], v[186:189], v[116:119]
	v_mfma_f32_16x16x32_bf16 v[104:107], v[124:127], v[186:189], v[104:107]
	v_mfma_f32_16x16x32_bf16 v[92:95], v[112:115], v[194:197], v[92:95]
	v_mfma_f32_16x16x32_bf16 v[88:91], v[124:127], v[194:197], v[88:91]
	v_mfma_f32_16x16x32_bf16 v[76:79], v[112:115], v[202:205], v[76:79]
	v_mfma_f32_16x16x32_bf16 v[72:75], v[124:127], v[202:205], v[72:75]
	s_setprio 0
	s_setprio 1
	v_mfma_f32_16x16x32_bf16 v[132:135], v[158:161], v[174:177], v[132:135]
	v_mfma_f32_16x16x32_bf16 v[128:131], v[166:169], v[174:177], v[128:131]
	v_mfma_f32_16x16x32_bf16 v[100:103], v[158:161], v[182:185], v[100:103]
	v_mfma_f32_16x16x32_bf16 v[96:99], v[166:169], v[182:185], v[96:99]
	v_mfma_f32_16x16x32_bf16 v[84:87], v[158:161], v[190:193], v[84:87]
	v_mfma_f32_16x16x32_bf16 v[80:83], v[166:169], v[190:193], v[80:83]
	v_mfma_f32_16x16x32_bf16 v[68:71], v[158:161], v[198:201], v[68:71]
	v_mfma_f32_16x16x32_bf16 v[64:67], v[166:169], v[198:201], v[64:67]
	v_mfma_f32_16x16x32_bf16 v[132:135], v[162:165], v[178:181], v[132:135]
	v_mfma_f32_16x16x32_bf16 v[128:131], v[170:173], v[178:181], v[128:131]
	v_mfma_f32_16x16x32_bf16 v[100:103], v[162:165], v[186:189], v[100:103]
	v_mfma_f32_16x16x32_bf16 v[96:99], v[170:173], v[186:189], v[96:99]
	v_mfma_f32_16x16x32_bf16 v[84:87], v[162:165], v[194:197], v[84:87]
	v_mfma_f32_16x16x32_bf16 v[80:83], v[170:173], v[194:197], v[80:83]
	v_mfma_f32_16x16x32_bf16 v[68:71], v[162:165], v[202:205], v[68:71]
	v_mfma_f32_16x16x32_bf16 v[64:67], v[170:173], v[202:205], v[64:67]
	s_setprio 0
	s_barrier
	s_mov_b32 m0, s30
	v_lshl_add_u64 v[206:207], s[50:51], 0, v[146:147]
	s_add_u32 s0, s50, 0x4000
	ds_read_b128 v[174:177], v157 offset:16384
	ds_read_b128 v[178:181], v157 offset:17408
	ds_read_b128 v[182:185], v157 offset:18432
	ds_read_b128 v[186:189], v157 offset:19456
	ds_read_b128 v[190:193], v157 offset:20480
	ds_read_b128 v[194:197], v157 offset:21504
	ds_read_b128 v[198:201], v157 offset:22528
	ds_read_b128 v[202:205], v157 offset:23552
	global_load_lds_dwordx4 v[206:207], off
	v_lshl_add_u64 v[206:207], s[50:51], 0, v[150:151]
	s_mov_b32 m0, s31
	s_addc_u32 s1, s51, 0
	global_load_lds_dwordx4 v[206:207], off
	v_lshl_add_u64 v[206:207], s[0:1], 0, v[146:147]
	s_mov_b32 m0, s54
	s_nop 0
	global_load_lds_dwordx4 v[206:207], off
	v_lshl_add_u64 v[206:207], s[0:1], 0, v[150:151]
	s_mov_b32 m0, s55
	s_nop 0
	global_load_lds_dwordx4 v[206:207], off
	v_lshl_add_u64 v[206:207], s[52:53], 0, v[144:145]
	s_mov_b32 m0, s56
	s_nop 0
	global_load_lds_dwordx4 v[206:207], off
	v_lshl_add_u64 v[206:207], s[52:53], 0, v[148:149]
	s_mov_b32 m0, s57
	s_nop 0
	global_load_lds_dwordx4 v[206:207], off
	s_waitcnt vmcnt(8)
	s_and_b64 vcc, exec, s[24:25]
	s_cbranch_vccnz .Llead_skip_2_1
	s_waitcnt lgkmcnt(0)
.Llead_skip_2_1:
	s_barrier
	s_setprio 1
	s_waitcnt lgkmcnt(0)
	v_mfma_f32_16x16x32_bf16 v[60:63], v[108:111], v[174:177], v[60:63]
	v_mfma_f32_16x16x32_bf16 v[56:59], v[120:123], v[174:177], v[56:59]
	v_mfma_f32_16x16x32_bf16 v[44:47], v[108:111], v[182:185], v[44:47]
	v_mfma_f32_16x16x32_bf16 v[40:43], v[120:123], v[182:185], v[40:43]
	v_mfma_f32_16x16x32_bf16 v[28:31], v[108:111], v[190:193], v[28:31]
	v_mfma_f32_16x16x32_bf16 v[24:27], v[120:123], v[190:193], v[24:27]
	v_mfma_f32_16x16x32_bf16 v[12:15], v[108:111], v[198:201], v[12:15]
	v_mfma_f32_16x16x32_bf16 v[8:11], v[120:123], v[198:201], v[8:11]
	v_mfma_f32_16x16x32_bf16 v[60:63], v[112:115], v[178:181], v[60:63]
	v_mfma_f32_16x16x32_bf16 v[56:59], v[124:127], v[178:181], v[56:59]
	v_mfma_f32_16x16x32_bf16 v[44:47], v[112:115], v[186:189], v[44:47]
	v_mfma_f32_16x16x32_bf16 v[40:43], v[124:127], v[186:189], v[40:43]
	v_mfma_f32_16x16x32_bf16 v[28:31], v[112:115], v[194:197], v[28:31]
	v_mfma_f32_16x16x32_bf16 v[24:27], v[124:127], v[194:197], v[24:27]
	v_mfma_f32_16x16x32_bf16 v[12:15], v[112:115], v[202:205], v[12:15]
	v_mfma_f32_16x16x32_bf16 v[8:11], v[124:127], v[202:205], v[8:11]
	s_setprio 0
	s_setprio 1
	v_mfma_f32_16x16x32_bf16 v[52:55], v[158:161], v[174:177], v[52:55]
	v_mfma_f32_16x16x32_bf16 v[48:51], v[166:169], v[174:177], v[48:51]
	v_mfma_f32_16x16x32_bf16 v[36:39], v[158:161], v[182:185], v[36:39]
	v_mfma_f32_16x16x32_bf16 v[32:35], v[166:169], v[182:185], v[32:35]
	v_mfma_f32_16x16x32_bf16 v[20:23], v[158:161], v[190:193], v[20:23]
	v_mfma_f32_16x16x32_bf16 v[16:19], v[166:169], v[190:193], v[16:19]
	v_mfma_f32_16x16x32_bf16 v[4:7], v[158:161], v[198:201], v[4:7]
	v_mfma_f32_16x16x32_bf16 v[0:3], v[166:169], v[198:201], v[0:3]
	v_mfma_f32_16x16x32_bf16 v[52:55], v[162:165], v[178:181], v[52:55]
	v_mfma_f32_16x16x32_bf16 v[48:51], v[170:173], v[178:181], v[48:51]
	v_mfma_f32_16x16x32_bf16 v[36:39], v[162:165], v[186:189], v[36:39]
	v_mfma_f32_16x16x32_bf16 v[32:35], v[170:173], v[186:189], v[32:35]
	v_mfma_f32_16x16x32_bf16 v[20:23], v[162:165], v[194:197], v[20:23]
	v_mfma_f32_16x16x32_bf16 v[16:19], v[170:173], v[194:197], v[16:19]
	v_mfma_f32_16x16x32_bf16 v[4:7], v[162:165], v[202:205], v[4:7]
	v_mfma_f32_16x16x32_bf16 v[0:3], v[170:173], v[202:205], v[0:3]
	s_setprio 0
	s_barrier
	v_add_u32_e32 v124, s62, v156
	v_add_u32_e32 v170, s67, v156
	ds_read_b128 v[108:111], v124
	ds_read_b128 v[112:115], v124 offset:1024
	ds_read_b128 v[120:123], v124 offset:2048
	ds_read_b128 v[124:127], v124 offset:3072
	ds_read_b128 v[158:161], v170
	ds_read_b128 v[162:165], v170 offset:1024
	ds_read_b128 v[166:169], v170 offset:2048
	ds_read_b128 v[170:173], v170 offset:3072
	s_add_u32 s0, s52, 0x4000
	s_addc_u32 s1, s53, 0
	s_mov_b32 m0, s58
	v_lshl_add_u64 v[206:207], s[0:1], 0, v[144:145]
	ds_read_b128 v[174:177], v157 offset:32768
	ds_read_b128 v[178:181], v157 offset:33792
	ds_read_b128 v[182:185], v157 offset:34816
	ds_read_b128 v[186:189], v157 offset:35840
	ds_read_b128 v[190:193], v157 offset:36864
	ds_read_b128 v[194:197], v157 offset:37888
	ds_read_b128 v[198:201], v157 offset:38912
	ds_read_b128 v[202:205], v157 offset:39936
	global_load_lds_dwordx4 v[206:207], off
	v_lshl_add_u64 v[206:207], s[0:1], 0, v[148:149]
	s_mov_b32 m0, s59
	s_nop 0
	global_load_lds_dwordx4 v[206:207], off
	s_waitcnt vmcnt(8)
	s_and_b64 vcc, exec, s[24:25]
	s_cbranch_vccnz .Llead_skip_2_2
	s_waitcnt lgkmcnt(0)
.Llead_skip_2_2:
	s_barrier
	s_setprio 1
	s_waitcnt lgkmcnt(0)
	v_mfma_f32_16x16x32_bf16 v[140:143], v[108:111], v[174:177], v[140:143]
	v_mfma_f32_16x16x32_bf16 v[136:139], v[120:123], v[174:177], v[136:139]
	v_mfma_f32_16x16x32_bf16 v[116:119], v[108:111], v[182:185], v[116:119]
	v_mfma_f32_16x16x32_bf16 v[104:107], v[120:123], v[182:185], v[104:107]
	v_mfma_f32_16x16x32_bf16 v[92:95], v[108:111], v[190:193], v[92:95]
	v_mfma_f32_16x16x32_bf16 v[88:91], v[120:123], v[190:193], v[88:91]
	v_mfma_f32_16x16x32_bf16 v[76:79], v[108:111], v[198:201], v[76:79]
	v_mfma_f32_16x16x32_bf16 v[72:75], v[120:123], v[198:201], v[72:75]
	v_mfma_f32_16x16x32_bf16 v[140:143], v[112:115], v[178:181], v[140:143]
	v_mfma_f32_16x16x32_bf16 v[136:139], v[124:127], v[178:181], v[136:139]
	v_mfma_f32_16x16x32_bf16 v[116:119], v[112:115], v[186:189], v[116:119]
	v_mfma_f32_16x16x32_bf16 v[104:107], v[124:127], v[186:189], v[104:107]
	v_mfma_f32_16x16x32_bf16 v[92:95], v[112:115], v[194:197], v[92:95]
	v_mfma_f32_16x16x32_bf16 v[88:91], v[124:127], v[194:197], v[88:91]
	v_mfma_f32_16x16x32_bf16 v[76:79], v[112:115], v[202:205], v[76:79]
	v_mfma_f32_16x16x32_bf16 v[72:75], v[124:127], v[202:205], v[72:75]
	s_setprio 0
	s_setprio 1
	v_mfma_f32_16x16x32_bf16 v[132:135], v[158:161], v[174:177], v[132:135]
	v_mfma_f32_16x16x32_bf16 v[128:131], v[166:169], v[174:177], v[128:131]
	v_mfma_f32_16x16x32_bf16 v[100:103], v[158:161], v[182:185], v[100:103]
	v_mfma_f32_16x16x32_bf16 v[96:99], v[166:169], v[182:185], v[96:99]
	v_mfma_f32_16x16x32_bf16 v[84:87], v[158:161], v[190:193], v[84:87]
	v_mfma_f32_16x16x32_bf16 v[80:83], v[166:169], v[190:193], v[80:83]
	v_mfma_f32_16x16x32_bf16 v[68:71], v[158:161], v[198:201], v[68:71]
	v_mfma_f32_16x16x32_bf16 v[64:67], v[166:169], v[198:201], v[64:67]
	v_mfma_f32_16x16x32_bf16 v[132:135], v[162:165], v[178:181], v[132:135]
	v_mfma_f32_16x16x32_bf16 v[128:131], v[170:173], v[178:181], v[128:131]
	v_mfma_f32_16x16x32_bf16 v[100:103], v[162:165], v[186:189], v[100:103]
	v_mfma_f32_16x16x32_bf16 v[96:99], v[170:173], v[186:189], v[96:99]
	v_mfma_f32_16x16x32_bf16 v[84:87], v[162:165], v[194:197], v[84:87]
	v_mfma_f32_16x16x32_bf16 v[80:83], v[170:173], v[194:197], v[80:83]
	v_mfma_f32_16x16x32_bf16 v[68:71], v[162:165], v[202:205], v[68:71]
	v_mfma_f32_16x16x32_bf16 v[64:67], v[170:173], v[202:205], v[64:67]
	s_setprio 0
	s_barrier
	s_add_u32 s0, s50, 0x8000
	s_addc_u32 s1, s51, 0
	s_mov_b32 m0, s63
	v_lshl_add_u64 v[206:207], s[0:1], 0, v[146:147]
	ds_read_b128 v[174:177], v157 offset:49152
	ds_read_b128 v[178:181], v157 offset:50176
	ds_read_b128 v[182:185], v157 offset:51200
	ds_read_b128 v[186:189], v157 offset:52224
	ds_read_b128 v[190:193], v157 offset:53248
	ds_read_b128 v[194:197], v157 offset:54272
	ds_read_b128 v[198:201], v157 offset:55296
	ds_read_b128 v[202:205], v157 offset:56320
	global_load_lds_dwordx4 v[206:207], off
	v_lshl_add_u64 v[206:207], s[0:1], 0, v[150:151]
	s_add_u32 s0, s50, 0xc000
	s_mov_b32 m0, s64
	s_addc_u32 s1, s51, 0
	global_load_lds_dwordx4 v[206:207], off
	v_lshl_add_u64 v[206:207], s[0:1], 0, v[146:147]
	s_mov_b32 m0, s68
	s_nop 0
	global_load_lds_dwordx4 v[206:207], off
	v_lshl_add_u64 v[206:207], s[0:1], 0, v[150:151]
	s_mov_b32 m0, s69
	s_nop 0
	global_load_lds_dwordx4 v[206:207], off
	v_lshl_add_u64 v[206:207], s[48:49], 0, v[144:145]
	s_mov_b32 m0, s65
	s_nop 0
	global_load_lds_dwordx4 v[206:207], off
	v_lshl_add_u64 v[206:207], s[48:49], 0, v[148:149]
	s_mov_b32 m0, s66
	s_nop 0
	global_load_lds_dwordx4 v[206:207], off
	s_waitcnt vmcnt(8)
	s_and_b64 vcc, exec, s[24:25]
	s_cbranch_vccnz .Llead_skip_2_3
	s_waitcnt lgkmcnt(0)
.Llead_skip_2_3:
	s_barrier
	s_setprio 1
	s_waitcnt lgkmcnt(0)
	v_mfma_f32_16x16x32_bf16 v[60:63], v[108:111], v[174:177], v[60:63]
	v_mfma_f32_16x16x32_bf16 v[56:59], v[120:123], v[174:177], v[56:59]
	v_mfma_f32_16x16x32_bf16 v[44:47], v[108:111], v[182:185], v[44:47]
	v_mfma_f32_16x16x32_bf16 v[40:43], v[120:123], v[182:185], v[40:43]
	v_mfma_f32_16x16x32_bf16 v[28:31], v[108:111], v[190:193], v[28:31]
	v_mfma_f32_16x16x32_bf16 v[24:27], v[120:123], v[190:193], v[24:27]
	v_mfma_f32_16x16x32_bf16 v[12:15], v[108:111], v[198:201], v[12:15]
	v_mfma_f32_16x16x32_bf16 v[8:11], v[120:123], v[198:201], v[8:11]
	v_mfma_f32_16x16x32_bf16 v[60:63], v[112:115], v[178:181], v[60:63]
	v_mfma_f32_16x16x32_bf16 v[56:59], v[124:127], v[178:181], v[56:59]
	v_mfma_f32_16x16x32_bf16 v[44:47], v[112:115], v[186:189], v[44:47]
	v_mfma_f32_16x16x32_bf16 v[40:43], v[124:127], v[186:189], v[40:43]
	v_mfma_f32_16x16x32_bf16 v[28:31], v[112:115], v[194:197], v[28:31]
	v_mfma_f32_16x16x32_bf16 v[24:27], v[124:127], v[194:197], v[24:27]
	v_mfma_f32_16x16x32_bf16 v[12:15], v[112:115], v[202:205], v[12:15]
	v_mfma_f32_16x16x32_bf16 v[8:11], v[124:127], v[202:205], v[8:11]
	s_setprio 0
	s_setprio 1
	v_mfma_f32_16x16x32_bf16 v[52:55], v[158:161], v[174:177], v[52:55]
	v_mfma_f32_16x16x32_bf16 v[48:51], v[166:169], v[174:177], v[48:51]
	v_mfma_f32_16x16x32_bf16 v[36:39], v[158:161], v[182:185], v[36:39]
	v_mfma_f32_16x16x32_bf16 v[32:35], v[166:169], v[182:185], v[32:35]
	v_mfma_f32_16x16x32_bf16 v[20:23], v[158:161], v[190:193], v[20:23]
	v_mfma_f32_16x16x32_bf16 v[16:19], v[166:169], v[190:193], v[16:19]
	v_mfma_f32_16x16x32_bf16 v[4:7], v[158:161], v[198:201], v[4:7]
	v_mfma_f32_16x16x32_bf16 v[0:3], v[166:169], v[198:201], v[0:3]
	v_mfma_f32_16x16x32_bf16 v[52:55], v[162:165], v[178:181], v[52:55]
	v_mfma_f32_16x16x32_bf16 v[48:51], v[170:173], v[178:181], v[48:51]
	v_mfma_f32_16x16x32_bf16 v[36:39], v[162:165], v[186:189], v[36:39]
	v_mfma_f32_16x16x32_bf16 v[32:35], v[170:173], v[186:189], v[32:35]
	v_mfma_f32_16x16x32_bf16 v[20:23], v[162:165], v[194:197], v[20:23]
	v_mfma_f32_16x16x32_bf16 v[16:19], v[170:173], v[194:197], v[16:19]
	v_mfma_f32_16x16x32_bf16 v[4:7], v[162:165], v[202:205], v[4:7]
	v_mfma_f32_16x16x32_bf16 v[0:3], v[170:173], v[202:205], v[0:3]
	s_setprio 0
	s_barrier
	s_add_i32 s78, s78, 2
	s_add_u32 s76, s76, 0x10000
	s_addc_u32 s77, s77, 0
	s_cmp_gt_u32 s78, 29
	s_mov_b64 s[0:1], s[46:47]
	s_cbranch_scc0 .LBB0_1173
	s_and_b64 vcc, exec, s[24:25]
	s_cbranch_vccz .LBB0_1176
	s_barrier

.LBB0_1248:
	v_add_u32_e32 v92, s30, v206
	v_add_u32_e32 v156, s52, v206
	ds_read_b128 v[72:75], v92
	ds_read_b128 v[76:79], v92 offset:1024
	ds_read_b128 v[84:87], v92 offset:2048
	ds_read_b128 v[92:95], v92 offset:3072
	ds_read_b128 v[144:147], v156
	ds_read_b128 v[148:151], v156 offset:1024
	ds_read_b128 v[152:155], v156 offset:2048
	ds_read_b128 v[156:159], v156 offset:3072
	s_add_u32 s44, s0, 0x10000
	s_addc_u32 s45, s1, 0
	s_cmpk_eq_i32 s76, 0x7c
	s_cselect_b32 s50, s5, s44
	s_cselect_b32 s51, s4, s45
	s_cselect_b32 s48, s35, s74
	s_cselect_b32 s49, s25, s75
	s_add_u32 s46, s50, 0x8000
	s_addc_u32 s47, s51, 0
	v_lshl_add_u64 v[204:205], s[0:1], 0, v[180:181]
	s_add_i32 m0, s56, 0xc000
	ds_read_b128 v[160:163], v207
	ds_read_b128 v[164:167], v207 offset:1024
	ds_read_b128 v[168:171], v207 offset:2048
	ds_read_b128 v[184:187], v207 offset:3072
	ds_read_b128 v[188:191], v207 offset:4096
	ds_read_b128 v[192:195], v207 offset:5120
	ds_read_b128 v[196:199], v207 offset:6144
	ds_read_b128 v[200:203], v207 offset:7168
	global_load_lds_dwordx4 v[204:205], off
	v_lshl_add_u64 v[204:205], s[0:1], 0, v[182:183]
	s_add_i32 m0, s56, 0xe000
	s_nop 0
	global_load_lds_dwordx4 v[204:205], off
	s_waitcnt vmcnt(8)
	s_and_b64 vcc, exec, s[22:23]
	s_cbranch_vccnz .Llead_skip_3_0
	s_waitcnt lgkmcnt(0)
.Llead_skip_3_0:
	s_barrier
	s_setprio 1
	s_waitcnt lgkmcnt(0)
	v_mfma_f32_16x16x32_bf16 v[140:143], v[72:75], v[160:163], v[140:143]
	v_mfma_f32_16x16x32_bf16 v[136:139], v[84:87], v[160:163], v[136:139]
	v_mfma_f32_16x16x32_bf16 v[124:127], v[72:75], v[168:171], v[124:127]
	v_mfma_f32_16x16x32_bf16 v[120:123], v[84:87], v[168:171], v[120:123]
	v_mfma_f32_16x16x32_bf16 v[108:111], v[72:75], v[188:191], v[108:111]
	v_mfma_f32_16x16x32_bf16 v[104:107], v[84:87], v[188:191], v[104:107]
	v_mfma_f32_16x16x32_bf16 v[88:91], v[72:75], v[196:199], v[88:91]
	v_mfma_f32_16x16x32_bf16 v[80:83], v[84:87], v[196:199], v[80:83]
	v_mfma_f32_16x16x32_bf16 v[140:143], v[76:79], v[164:167], v[140:143]
	v_mfma_f32_16x16x32_bf16 v[136:139], v[92:95], v[164:167], v[136:139]
	v_mfma_f32_16x16x32_bf16 v[124:127], v[76:79], v[184:187], v[124:127]
	v_mfma_f32_16x16x32_bf16 v[120:123], v[92:95], v[184:187], v[120:123]
	v_mfma_f32_16x16x32_bf16 v[108:111], v[76:79], v[192:195], v[108:111]
	v_mfma_f32_16x16x32_bf16 v[104:107], v[92:95], v[192:195], v[104:107]
	v_mfma_f32_16x16x32_bf16 v[88:91], v[76:79], v[200:203], v[88:91]
	v_mfma_f32_16x16x32_bf16 v[80:83], v[92:95], v[200:203], v[80:83]
	s_setprio 0
	s_setprio 1
	v_mfma_f32_16x16x32_bf16 v[132:135], v[144:147], v[160:163], v[132:135]
	v_mfma_f32_16x16x32_bf16 v[128:131], v[152:155], v[160:163], v[128:131]
	v_mfma_f32_16x16x32_bf16 v[116:119], v[144:147], v[168:171], v[116:119]
	v_mfma_f32_16x16x32_bf16 v[112:115], v[152:155], v[168:171], v[112:115]
	v_mfma_f32_16x16x32_bf16 v[100:103], v[144:147], v[188:191], v[100:103]
	v_mfma_f32_16x16x32_bf16 v[96:99], v[152:155], v[188:191], v[96:99]
	v_mfma_f32_16x16x32_bf16 v[68:71], v[144:147], v[196:199], v[68:71]
	v_mfma_f32_16x16x32_bf16 v[64:67], v[152:155], v[196:199], v[64:67]
	v_mfma_f32_16x16x32_bf16 v[132:135], v[148:151], v[164:167], v[132:135]
	v_mfma_f32_16x16x32_bf16 v[128:131], v[156:159], v[164:167], v[128:131]
	v_mfma_f32_16x16x32_bf16 v[116:119], v[148:151], v[184:187], v[116:119]
	v_mfma_f32_16x16x32_bf16 v[112:115], v[156:159], v[184:187], v[112:115]
	v_mfma_f32_16x16x32_bf16 v[100:103], v[148:151], v[192:195], v[100:103]
	v_mfma_f32_16x16x32_bf16 v[96:99], v[156:159], v[192:195], v[96:99]
	v_mfma_f32_16x16x32_bf16 v[68:71], v[148:151], v[200:203], v[68:71]
	v_mfma_f32_16x16x32_bf16 v[64:67], v[156:159], v[200:203], v[64:67]
	s_setprio 0
	s_barrier
	s_mov_b32 m0, s31
	v_lshl_add_u64 v[204:205], s[48:49], 0, v[174:175]
	s_add_u32 s0, s48, 0x4000
	ds_read_b128 v[160:163], v207 offset:16384
	ds_read_b128 v[164:167], v207 offset:17408
	ds_read_b128 v[168:171], v207 offset:18432
	ds_read_b128 v[184:187], v207 offset:19456
	ds_read_b128 v[188:191], v207 offset:20480
	ds_read_b128 v[192:195], v207 offset:21504
	ds_read_b128 v[196:199], v207 offset:22528
	ds_read_b128 v[200:203], v207 offset:23552
	global_load_lds_dwordx4 v[204:205], off
	v_lshl_add_u64 v[204:205], s[48:49], 0, v[178:179]
	s_mov_b32 m0, s43
	s_addc_u32 s1, s49, 0
	global_load_lds_dwordx4 v[204:205], off
	v_lshl_add_u64 v[204:205], s[0:1], 0, v[174:175]
	s_mov_b32 m0, s53
	s_nop 0
	global_load_lds_dwordx4 v[204:205], off
	v_lshl_add_u64 v[204:205], s[0:1], 0, v[178:179]
	s_mov_b32 m0, s54
	s_nop 0
	global_load_lds_dwordx4 v[204:205], off
	v_lshl_add_u64 v[204:205], s[50:51], 0, v[172:173]
	s_mov_b32 m0, s56
	s_nop 0
	global_load_lds_dwordx4 v[204:205], off
	v_lshl_add_u64 v[204:205], s[50:51], 0, v[176:177]
	s_mov_b32 m0, s57
	s_nop 0
	global_load_lds_dwordx4 v[204:205], off
	s_waitcnt vmcnt(8)
	s_and_b64 vcc, exec, s[22:23]
	s_cbranch_vccnz .Llead_skip_3_1
	s_waitcnt lgkmcnt(0)
.Llead_skip_3_1:
	s_barrier
	s_setprio 1
	s_waitcnt lgkmcnt(0)
	v_mfma_f32_16x16x32_bf16 v[60:63], v[72:75], v[160:163], v[60:63]
	v_mfma_f32_16x16x32_bf16 v[56:59], v[84:87], v[160:163], v[56:59]
	v_mfma_f32_16x16x32_bf16 v[44:47], v[72:75], v[168:171], v[44:47]
	v_mfma_f32_16x16x32_bf16 v[40:43], v[84:87], v[168:171], v[40:43]
	v_mfma_f32_16x16x32_bf16 v[28:31], v[72:75], v[188:191], v[28:31]
	v_mfma_f32_16x16x32_bf16 v[24:27], v[84:87], v[188:191], v[24:27]
	v_mfma_f32_16x16x32_bf16 v[12:15], v[72:75], v[196:199], v[12:15]
	v_mfma_f32_16x16x32_bf16 v[8:11], v[84:87], v[196:199], v[8:11]
	v_mfma_f32_16x16x32_bf16 v[60:63], v[76:79], v[164:167], v[60:63]
	v_mfma_f32_16x16x32_bf16 v[56:59], v[92:95], v[164:167], v[56:59]
	v_mfma_f32_16x16x32_bf16 v[44:47], v[76:79], v[184:187], v[44:47]
	v_mfma_f32_16x16x32_bf16 v[40:43], v[92:95], v[184:187], v[40:43]
	v_mfma_f32_16x16x32_bf16 v[28:31], v[76:79], v[192:195], v[28:31]
	v_mfma_f32_16x16x32_bf16 v[24:27], v[92:95], v[192:195], v[24:27]
	v_mfma_f32_16x16x32_bf16 v[12:15], v[76:79], v[200:203], v[12:15]
	v_mfma_f32_16x16x32_bf16 v[8:11], v[92:95], v[200:203], v[8:11]
	s_setprio 0
	s_setprio 1
	v_mfma_f32_16x16x32_bf16 v[52:55], v[144:147], v[160:163], v[52:55]
	v_mfma_f32_16x16x32_bf16 v[48:51], v[152:155], v[160:163], v[48:51]
	v_mfma_f32_16x16x32_bf16 v[36:39], v[144:147], v[168:171], v[36:39]
	v_mfma_f32_16x16x32_bf16 v[32:35], v[152:155], v[168:171], v[32:35]
	v_mfma_f32_16x16x32_bf16 v[20:23], v[144:147], v[188:191], v[20:23]
	v_mfma_f32_16x16x32_bf16 v[16:19], v[152:155], v[188:191], v[16:19]
	v_mfma_f32_16x16x32_bf16 v[4:7], v[144:147], v[196:199], v[4:7]
	v_mfma_f32_16x16x32_bf16 v[0:3], v[152:155], v[196:199], v[0:3]
	v_mfma_f32_16x16x32_bf16 v[52:55], v[148:151], v[164:167], v[52:55]
	v_mfma_f32_16x16x32_bf16 v[48:51], v[156:159], v[164:167], v[48:51]
	v_mfma_f32_16x16x32_bf16 v[36:39], v[148:151], v[184:187], v[36:39]
	v_mfma_f32_16x16x32_bf16 v[32:35], v[156:159], v[184:187], v[32:35]
	v_mfma_f32_16x16x32_bf16 v[20:23], v[148:151], v[192:195], v[20:23]
	v_mfma_f32_16x16x32_bf16 v[16:19], v[156:159], v[192:195], v[16:19]
	v_mfma_f32_16x16x32_bf16 v[4:7], v[148:151], v[200:203], v[4:7]
	v_mfma_f32_16x16x32_bf16 v[0:3], v[156:159], v[200:203], v[0:3]
	s_setprio 0
	s_barrier
	v_add_u32_e32 v92, s64, v206
	v_add_u32_e32 v156, s69, v206
	ds_read_b128 v[72:75], v92
	ds_read_b128 v[76:79], v92 offset:1024
	ds_read_b128 v[84:87], v92 offset:2048
	ds_read_b128 v[92:95], v92 offset:3072
	ds_read_b128 v[144:147], v156
	ds_read_b128 v[148:151], v156 offset:1024
	ds_read_b128 v[152:155], v156 offset:2048
	ds_read_b128 v[156:159], v156 offset:3072
	s_add_u32 s0, s50, 0x4000
	s_addc_u32 s1, s51, 0
	s_mov_b32 m0, s58
	v_lshl_add_u64 v[204:205], s[0:1], 0, v[172:173]
	ds_read_b128 v[160:163], v207 offset:32768
	ds_read_b128 v[164:167], v207 offset:33792
	ds_read_b128 v[168:171], v207 offset:34816
	ds_read_b128 v[184:187], v207 offset:35840
	ds_read_b128 v[188:191], v207 offset:36864
	ds_read_b128 v[192:195], v207 offset:37888
	ds_read_b128 v[196:199], v207 offset:38912
	ds_read_b128 v[200:203], v207 offset:39936
	global_load_lds_dwordx4 v[204:205], off
	v_lshl_add_u64 v[204:205], s[0:1], 0, v[176:177]
	s_mov_b32 m0, s59
	s_nop 0
	global_load_lds_dwordx4 v[204:205], off
	s_waitcnt vmcnt(8)
	s_and_b64 vcc, exec, s[22:23]
	s_cbranch_vccnz .Llead_skip_3_2
	s_waitcnt lgkmcnt(0)
.Llead_skip_3_2:
	s_barrier
	s_setprio 1
	s_waitcnt lgkmcnt(0)
	v_mfma_f32_16x16x32_bf16 v[140:143], v[72:75], v[160:163], v[140:143]
	v_mfma_f32_16x16x32_bf16 v[136:139], v[84:87], v[160:163], v[136:139]
	v_mfma_f32_16x16x32_bf16 v[124:127], v[72:75], v[168:171], v[124:127]
	v_mfma_f32_16x16x32_bf16 v[120:123], v[84:87], v[168:171], v[120:123]
	v_mfma_f32_16x16x32_bf16 v[108:111], v[72:75], v[188:191], v[108:111]
	v_mfma_f32_16x16x32_bf16 v[104:107], v[84:87], v[188:191], v[104:107]
	v_mfma_f32_16x16x32_bf16 v[88:91], v[72:75], v[196:199], v[88:91]
	v_mfma_f32_16x16x32_bf16 v[80:83], v[84:87], v[196:199], v[80:83]
	v_mfma_f32_16x16x32_bf16 v[140:143], v[76:79], v[164:167], v[140:143]
	v_mfma_f32_16x16x32_bf16 v[136:139], v[92:95], v[164:167], v[136:139]
	v_mfma_f32_16x16x32_bf16 v[124:127], v[76:79], v[184:187], v[124:127]
	v_mfma_f32_16x16x32_bf16 v[120:123], v[92:95], v[184:187], v[120:123]
	v_mfma_f32_16x16x32_bf16 v[108:111], v[76:79], v[192:195], v[108:111]
	v_mfma_f32_16x16x32_bf16 v[104:107], v[92:95], v[192:195], v[104:107]
	v_mfma_f32_16x16x32_bf16 v[88:91], v[76:79], v[200:203], v[88:91]
	v_mfma_f32_16x16x32_bf16 v[80:83], v[92:95], v[200:203], v[80:83]
	s_setprio 0
	s_setprio 1
	v_mfma_f32_16x16x32_bf16 v[132:135], v[144:147], v[160:163], v[132:135]
	v_mfma_f32_16x16x32_bf16 v[128:131], v[152:155], v[160:163], v[128:131]
	v_mfma_f32_16x16x32_bf16 v[116:119], v[144:147], v[168:171], v[116:119]
	v_mfma_f32_16x16x32_bf16 v[112:115], v[152:155], v[168:171], v[112:115]
	v_mfma_f32_16x16x32_bf16 v[100:103], v[144:147], v[188:191], v[100:103]
	v_mfma_f32_16x16x32_bf16 v[96:99], v[152:155], v[188:191], v[96:99]
	v_mfma_f32_16x16x32_bf16 v[68:71], v[144:147], v[196:199], v[68:71]
	v_mfma_f32_16x16x32_bf16 v[64:67], v[152:155], v[196:199], v[64:67]
	v_mfma_f32_16x16x32_bf16 v[132:135], v[148:151], v[164:167], v[132:135]
	v_mfma_f32_16x16x32_bf16 v[128:131], v[156:159], v[164:167], v[128:131]
	v_mfma_f32_16x16x32_bf16 v[116:119], v[148:151], v[184:187], v[116:119]
	v_mfma_f32_16x16x32_bf16 v[112:115], v[156:159], v[184:187], v[112:115]
	v_mfma_f32_16x16x32_bf16 v[100:103], v[148:151], v[192:195], v[100:103]
	v_mfma_f32_16x16x32_bf16 v[96:99], v[156:159], v[192:195], v[96:99]
	v_mfma_f32_16x16x32_bf16 v[68:71], v[148:151], v[200:203], v[68:71]
	v_mfma_f32_16x16x32_bf16 v[64:67], v[156:159], v[200:203], v[64:67]
	s_setprio 0
	s_barrier
	s_add_u32 s0, s48, 0x8000
	s_addc_u32 s1, s49, 0
	s_mov_b32 m0, s65
	v_lshl_add_u64 v[204:205], s[0:1], 0, v[174:175]
	ds_read_b128 v[160:163], v207 offset:49152
	ds_read_b128 v[164:167], v207 offset:50176
	ds_read_b128 v[168:171], v207 offset:51200
	ds_read_b128 v[184:187], v207 offset:52224
	ds_read_b128 v[188:191], v207 offset:53248
	ds_read_b128 v[192:195], v207 offset:54272
	ds_read_b128 v[196:199], v207 offset:55296
	ds_read_b128 v[200:203], v207 offset:56320
	global_load_lds_dwordx4 v[204:205], off
	v_lshl_add_u64 v[204:205], s[0:1], 0, v[178:179]
	s_add_u32 s0, s48, 0xc000
	s_mov_b32 m0, s66
	s_addc_u32 s1, s49, 0
	global_load_lds_dwordx4 v[204:205], off
	v_lshl_add_u64 v[204:205], s[0:1], 0, v[174:175]
	s_mov_b32 m0, s70
	s_nop 0
	global_load_lds_dwordx4 v[204:205], off
	v_lshl_add_u64 v[204:205], s[0:1], 0, v[178:179]
	s_mov_b32 m0, s71
	s_nop 0
	global_load_lds_dwordx4 v[204:205], off
	v_lshl_add_u64 v[204:205], s[46:47], 0, v[172:173]
	s_mov_b32 m0, s67
	s_nop 0
	global_load_lds_dwordx4 v[204:205], off
	v_lshl_add_u64 v[204:205], s[46:47], 0, v[176:177]
	s_mov_b32 m0, s68
	s_nop 0
	global_load_lds_dwordx4 v[204:205], off
	s_waitcnt vmcnt(8)
	s_and_b64 vcc, exec, s[22:23]
	s_cbranch_vccnz .Llead_skip_3_3
	s_waitcnt lgkmcnt(0)
.Llead_skip_3_3:
	s_barrier
	s_setprio 1
	s_waitcnt lgkmcnt(0)
	v_mfma_f32_16x16x32_bf16 v[60:63], v[72:75], v[160:163], v[60:63]
	v_mfma_f32_16x16x32_bf16 v[56:59], v[84:87], v[160:163], v[56:59]
	v_mfma_f32_16x16x32_bf16 v[44:47], v[72:75], v[168:171], v[44:47]
	v_mfma_f32_16x16x32_bf16 v[40:43], v[84:87], v[168:171], v[40:43]
	v_mfma_f32_16x16x32_bf16 v[28:31], v[72:75], v[188:191], v[28:31]
	v_mfma_f32_16x16x32_bf16 v[24:27], v[84:87], v[188:191], v[24:27]
	v_mfma_f32_16x16x32_bf16 v[12:15], v[72:75], v[196:199], v[12:15]
	v_mfma_f32_16x16x32_bf16 v[8:11], v[84:87], v[196:199], v[8:11]
	v_mfma_f32_16x16x32_bf16 v[60:63], v[76:79], v[164:167], v[60:63]
	v_mfma_f32_16x16x32_bf16 v[56:59], v[92:95], v[164:167], v[56:59]
	v_mfma_f32_16x16x32_bf16 v[44:47], v[76:79], v[184:187], v[44:47]
	v_mfma_f32_16x16x32_bf16 v[40:43], v[92:95], v[184:187], v[40:43]
	v_mfma_f32_16x16x32_bf16 v[28:31], v[76:79], v[192:195], v[28:31]
	v_mfma_f32_16x16x32_bf16 v[24:27], v[92:95], v[192:195], v[24:27]
	v_mfma_f32_16x16x32_bf16 v[12:15], v[76:79], v[200:203], v[12:15]
	v_mfma_f32_16x16x32_bf16 v[8:11], v[92:95], v[200:203], v[8:11]
	s_setprio 0
	s_setprio 1
	v_mfma_f32_16x16x32_bf16 v[52:55], v[144:147], v[160:163], v[52:55]
	v_mfma_f32_16x16x32_bf16 v[48:51], v[152:155], v[160:163], v[48:51]
	v_mfma_f32_16x16x32_bf16 v[36:39], v[144:147], v[168:171], v[36:39]
	v_mfma_f32_16x16x32_bf16 v[32:35], v[152:155], v[168:171], v[32:35]
	v_mfma_f32_16x16x32_bf16 v[20:23], v[144:147], v[188:191], v[20:23]
	v_mfma_f32_16x16x32_bf16 v[16:19], v[152:155], v[188:191], v[16:19]
	v_mfma_f32_16x16x32_bf16 v[4:7], v[144:147], v[196:199], v[4:7]
	v_mfma_f32_16x16x32_bf16 v[0:3], v[152:155], v[196:199], v[0:3]
	v_mfma_f32_16x16x32_bf16 v[52:55], v[148:151], v[164:167], v[52:55]
	v_mfma_f32_16x16x32_bf16 v[48:51], v[156:159], v[164:167], v[48:51]
	v_mfma_f32_16x16x32_bf16 v[36:39], v[148:151], v[184:187], v[36:39]
	v_mfma_f32_16x16x32_bf16 v[32:35], v[156:159], v[184:187], v[32:35]
	v_mfma_f32_16x16x32_bf16 v[20:23], v[148:151], v[192:195], v[20:23]
	v_mfma_f32_16x16x32_bf16 v[16:19], v[156:159], v[192:195], v[16:19]
	v_mfma_f32_16x16x32_bf16 v[4:7], v[148:151], v[200:203], v[4:7]
	v_mfma_f32_16x16x32_bf16 v[0:3], v[156:159], v[200:203], v[0:3]
	s_setprio 0
	s_barrier
	s_add_i32 s76, s76, 2
	s_add_u32 s74, s74, 0x10000
	s_addc_u32 s75, s75, 0
	s_cmpk_gt_u32 s76, 0x7d
	s_mov_b64 s[0:1], s[44:45]
	s_cbranch_scc0 .LBB0_1248
	s_and_b64 vcc, exec, s[22:23]
	s_cbranch_vccz .LBB0_1251
	s_barrier
